# ROUTE LayerNorm loop: counted waits step over the other half's 8 stores (N+8) except on the first X half and the last Y half
# baseline (speedup 1.0000x reference)
.LBB0_608:
	s_add_i32 s50, s50, 2
	s_cmp_eq_u32 s50, 8
	s_cbranch_scc1 .Lly_f0
	s_waitcnt vmcnt(21)
	s_branch .Lly_d0
.Lly_f0:
	s_waitcnt vmcnt(13)
.Lly_d0:
	v_lshlrev_b32_e32 v112, 16, v62
	v_and_b32_e32 v113, 0xffff0000, v62
	v_lshlrev_b32_e32 v62, 16, v63
	v_and_b32_e32 v63, 0xffff0000, v63
	v_lshlrev_b32_e32 v114, 16, v58
	v_and_b32_e32 v115, 0xffff0000, v58
	v_lshlrev_b32_e32 v58, 16, v59
	v_and_b32_e32 v59, 0xffff0000, v59
	v_pk_fma_f32 v[62:63], v[62:63], s[90:91], v[58:59] op_sel_hi:[1,0,1]
	v_pk_fma_f32 v[112:113], v[112:113], s[90:91], v[114:115] op_sel_hi:[1,0,1]
	v_lshlrev_b32_e32 v58, 16, v64
	v_and_b32_e32 v59, 0xffff0000, v64
	v_lshlrev_b32_e32 v64, 16, v65
	v_and_b32_e32 v65, 0xffff0000, v65
	v_lshlrev_b32_e32 v114, 16, v60
	v_and_b32_e32 v115, 0xffff0000, v60
	v_lshlrev_b32_e32 v60, 16, v61
	v_and_b32_e32 v61, 0xffff0000, v61
	v_pk_fma_f32 v[60:61], v[64:65], s[90:91], v[60:61] op_sel_hi:[1,0,1]
	v_pk_fma_f32 v[64:65], v[58:59], s[90:91], v[114:115] op_sel_hi:[1,0,1]
	v_mov_b32_e32 v58, v112
	v_mov_b32_e32 v59, v64
	v_mov_b32_e32 v114, v113
	v_mov_b32_e32 v115, v65
	v_pk_add_f32 v[58:59], v[58:59], v[114:115]
	v_mov_b32_e32 v114, v62
	v_mov_b32_e32 v115, v60
	v_mov_b32_e32 v116, v63
	v_mov_b32_e32 v117, v61
	v_pk_add_f32 v[114:115], v[114:115], v[116:117]
	v_lshlrev_b32_e32 v116, 16, v50
	v_pk_add_f32 v[58:59], v[58:59], v[114:115]
	v_and_b32_e32 v117, 0xffff0000, v50
	v_pk_add_f32 v[114:115], v[58:59], v[58:59] op_sel:[0,1] op_sel_hi:[1,0]
	s_cmp_eq_u32 s50, 8
	s_cbranch_scc1 .Lly_f1
	s_waitcnt vmcnt(20)
	s_branch .Lly_d1

.Lly_d1:
	v_lshlrev_b32_e32 v58, 16, v54
	v_and_b32_e32 v59, 0xffff0000, v54
	v_lshlrev_b32_e32 v54, 16, v55
	v_and_b32_e32 v55, 0xffff0000, v55
	v_lshlrev_b32_e32 v50, 16, v51
	v_and_b32_e32 v51, 0xffff0000, v51
	v_pk_fma_f32 v[54:55], v[54:55], s[90:91], v[50:51] op_sel_hi:[1,0,1]
	v_pk_fma_f32 v[58:59], v[58:59], s[90:91], v[116:117] op_sel_hi:[1,0,1]
	v_lshlrev_b32_e32 v50, 16, v56
	v_and_b32_e32 v51, 0xffff0000, v56
	v_lshlrev_b32_e32 v56, 16, v57
	v_and_b32_e32 v57, 0xffff0000, v57
	v_lshlrev_b32_e32 v116, 16, v52
	v_and_b32_e32 v117, 0xffff0000, v52
	v_lshlrev_b32_e32 v52, 16, v53
	v_and_b32_e32 v53, 0xffff0000, v53
	v_pk_fma_f32 v[52:53], v[56:57], s[90:91], v[52:53] op_sel_hi:[1,0,1]
	v_pk_fma_f32 v[56:57], v[50:51], s[90:91], v[116:117] op_sel_hi:[1,0,1]
	v_pk_mov_b32 v[50:51], v[58:59], v[54:55] op_sel:[1,0]
	v_mov_b32_e32 v116, v58
	v_mov_b32_e32 v117, v55
	v_pk_add_f32 v[50:51], v[50:51], v[116:117]
	v_mov_b32_e32 v118, v56
	v_pk_add_f32 v[116:117], v[50:51], v[50:51] op_sel:[0,1] op_sel_hi:[1,0]
	v_pk_mov_b32 v[50:51], v[56:57], v[52:53] op_sel:[1,0]
	v_mov_b32_e32 v119, v53
	v_pk_add_f32 v[50:51], v[50:51], v[118:119]
	s_cmp_eq_u32 s50, 8
	s_cbranch_scc1 .Lly_f2
	s_waitcnt vmcnt(19)
	s_branch .Lly_d2
.Lly_f2:
	s_waitcnt vmcnt(11)
.Lly_d2:
	v_lshlrev_b32_e32 v120, 16, v42
	v_pk_add_f32 v[118:119], v[50:51], v[50:51] op_sel:[0,1] op_sel_hi:[1,0]
	s_cmp_eq_u32 s50, 8
	s_cbranch_scc1 .Lly_f3
	s_waitcnt vmcnt(17)
	s_branch .Lly_d3
.Lly_f3:
	s_waitcnt vmcnt(9)
.Lly_d3:
	v_lshlrev_b32_e32 v50, 16, v46
	v_and_b32_e32 v51, 0xffff0000, v46
	v_lshlrev_b32_e32 v46, 16, v47
	v_and_b32_e32 v47, 0xffff0000, v47
	v_and_b32_e32 v121, 0xffff0000, v42
	v_lshlrev_b32_e32 v42, 16, v43
	v_and_b32_e32 v43, 0xffff0000, v43
	v_pk_fma_f32 v[46:47], v[46:47], s[90:91], v[42:43] op_sel_hi:[1,0,1]
	v_pk_fma_f32 v[50:51], v[50:51], s[90:91], v[120:121] op_sel_hi:[1,0,1]
	v_lshlrev_b32_e32 v42, 16, v48
	v_and_b32_e32 v43, 0xffff0000, v48
	v_lshlrev_b32_e32 v48, 16, v49
	v_and_b32_e32 v49, 0xffff0000, v49
	v_lshlrev_b32_e32 v120, 16, v44
	v_and_b32_e32 v121, 0xffff0000, v44
	v_lshlrev_b32_e32 v44, 16, v45
	v_and_b32_e32 v45, 0xffff0000, v45
	v_pk_fma_f32 v[44:45], v[48:49], s[90:91], v[44:45] op_sel_hi:[1,0,1]
	v_pk_fma_f32 v[48:49], v[42:43], s[90:91], v[120:121] op_sel_hi:[1,0,1]
	s_cmp_eq_u32 s50, 8
	s_cbranch_scc1 .Lly_f4
	s_waitcnt vmcnt(16)
	s_branch .Lly_d4

.Lly_d4:
	v_lshlrev_b32_e32 v42, 16, v38
	v_and_b32_e32 v43, 0xffff0000, v38
	v_lshlrev_b32_e32 v38, 16, v39
	v_and_b32_e32 v39, 0xffff0000, v39
	v_lshlrev_b32_e32 v128, 16, v34
	v_and_b32_e32 v129, 0xffff0000, v34
	v_lshlrev_b32_e32 v34, 16, v35
	v_and_b32_e32 v35, 0xffff0000, v35
	v_pk_fma_f32 v[38:39], v[38:39], s[90:91], v[34:35] op_sel_hi:[1,0,1]
	v_pk_fma_f32 v[42:43], v[42:43], s[90:91], v[128:129] op_sel_hi:[1,0,1]
	v_lshlrev_b32_e32 v128, 16, v40
	v_and_b32_e32 v129, 0xffff0000, v40
	v_lshlrev_b32_e32 v34, 16, v41
	v_and_b32_e32 v35, 0xffff0000, v41
	v_lshlrev_b32_e32 v40, 16, v36
	v_and_b32_e32 v41, 0xffff0000, v36
	v_lshlrev_b32_e32 v36, 16, v37
	v_and_b32_e32 v37, 0xffff0000, v37
	v_pk_fma_f32 v[34:35], v[34:35], s[90:91], v[36:37] op_sel_hi:[1,0,1]
	v_pk_fma_f32 v[36:37], v[128:129], s[90:91], v[40:41] op_sel_hi:[1,0,1]
	v_mov_b32_e32 v115, v42
	v_mov_b32_e32 v40, v1
	v_mov_b32_e32 v41, v43
	v_mov_b32_e32 v117, v38
	v_mov_b32_e32 v119, v39
	v_add_f32_e32 v120, v50, v51
	v_add_f32_e32 v122, v46, v47
	v_add_f32_e32 v124, v48, v49
	v_add_f32_e32 v126, v44, v45
	v_pk_add_f32 v[40:41], v[114:115], v[40:41]
	v_pk_add_f32 v[114:115], v[116:117], v[118:119]
	v_mov_b32_e32 v121, v36
	v_mov_b32_e32 v123, v37
	v_mov_b32_e32 v125, v34
	v_mov_b32_e32 v127, v35
	v_pk_add_f32 v[40:41], v[40:41], v[114:115]
	v_pk_add_f32 v[114:115], v[120:121], v[122:123]
	v_pk_add_f32 v[116:117], v[124:125], v[126:127]
	s_nop 0
	v_pk_add_f32 v[114:115], v[114:115], v[116:117]
	s_nop 0
	v_pk_add_f32 v[40:41], v[40:41], v[114:115]
	s_nop 0
	v_add_f32_e32 v0, v40, v41
	ds_bpermute_b32 v40, v146, v0
	s_waitcnt lgkmcnt(0)
	v_add_f32_e32 v0, v0, v40
	ds_bpermute_b32 v40, v147, v0
	s_waitcnt lgkmcnt(0)
	v_add_f32_e32 v0, v0, v40
	ds_bpermute_b32 v40, v148, v0
	s_waitcnt lgkmcnt(0)
	v_add_f32_e32 v0, v0, v40
	ds_bpermute_b32 v40, v149, v0
	s_waitcnt lgkmcnt(0)
	v_add_f32_e32 v0, v0, v40
	ds_bpermute_b32 v40, v150, v0
	s_waitcnt lgkmcnt(0)
	v_add_f32_e32 v0, v0, v40
	ds_bpermute_b32 v40, v151, v0
	s_waitcnt lgkmcnt(0)
	v_add_f32_e32 v120, v0, v40
	v_fmamk_f32 v113, v120, 0xba000000, v113
	v_fmamk_f32 v65, v120, 0xba000000, v65
	v_fmamk_f32 v63, v120, 0xba000000, v63
	v_fmac_f32_e32 v112, 0xba000000, v120
	v_fmamk_f32 v61, v120, 0xba000000, v61
	v_fmac_f32_e32 v64, 0xba000000, v120
	v_mov_b32_e32 v114, v113
	v_mov_b32_e32 v115, v65
	v_fmac_f32_e32 v62, 0xba000000, v120
	v_fmac_f32_e32 v60, 0xba000000, v120
	v_mov_b32_e32 v40, v112
	v_mov_b32_e32 v41, v64
	v_pk_mul_f32 v[114:115], v[114:115], v[114:115]
	v_mov_b32_e32 v116, v63
	v_mov_b32_e32 v117, v61
	v_pk_fma_f32 v[40:41], v[40:41], v[40:41], v[114:115]
	v_mov_b32_e32 v114, v62
	v_mov_b32_e32 v115, v60
	v_pk_mul_f32 v[116:117], v[116:117], v[116:117]
	v_fmamk_f32 v59, v120, 0xba000000, v59
	v_pk_fma_f32 v[114:115], v[114:115], v[114:115], v[116:117]
	v_fmac_f32_e32 v58, 0xba000000, v120
	v_fmamk_f32 v55, v120, 0xba000000, v55
	v_fmac_f32_e32 v54, 0xba000000, v120
	v_pk_add_f32 v[40:41], v[40:41], v[114:115]
	v_pk_mul_f32 v[114:115], v[54:55], v[54:55]
	v_pk_mul_f32 v[116:117], v[58:59], v[58:59]
	v_fmac_f32_e32 v56, 0xba000000, v120
	v_pk_mov_b32 v[118:119], v[116:117], v[114:115] op_sel:[1,0]
	v_mov_b32_e32 v117, v115
	v_fmamk_f32 v57, v120, 0xba000000, v57
	v_fmac_f32_e32 v52, 0xba000000, v120
	v_mul_f32_e32 v0, v56, v56
	v_pk_add_f32 v[114:115], v[118:119], v[116:117]
	v_fmamk_f32 v53, v120, 0xba000000, v53
	v_pk_fma_f32 v[116:117], v[56:57], v[56:57], v[0:1] op_sel_hi:[1,1,0]
	v_mul_f32_e32 v0, v52, v52
	v_pk_add_f32 v[40:41], v[40:41], v[40:41] op_sel_hi:[0,1]
	v_pk_add_f32 v[114:115], v[114:115], v[114:115] op_sel_hi:[0,1]
	v_pk_fma_f32 v[118:119], v[52:53], v[52:53], v[0:1] op_sel_hi:[1,1,0]
	v_fmamk_f32 v47, v120, 0xba000000, v47
	v_fmac_f32_e32 v46, 0xba000000, v120
	v_fmamk_f32 v51, v120, 0xba000000, v51
	v_fmac_f32_e32 v50, 0xba000000, v120
	v_mul_f32_e32 v116, v50, v50
	v_mul_f32_e32 v118, v51, v51
	v_mul_f32_e32 v114, v46, v46
	v_mul_f32_e32 v40, v47, v47
	v_pk_add_f32 v[116:117], v[116:117], v[118:119]
	v_pk_add_f32 v[40:41], v[114:115], v[40:41]
	v_fmamk_f32 v49, v120, 0xba000000, v49
	v_fmac_f32_e32 v48, 0xba000000, v120
	v_fmamk_f32 v45, v120, 0xba000000, v45
	v_fmac_f32_e32 v44, 0xba000000, v120
	v_pk_add_f32 v[40:41], v[116:117], v[40:41]
	v_pk_mul_f32 v[114:115], v[44:45], v[44:45]
	v_pk_mul_f32 v[116:117], v[48:49], v[48:49]
	v_fmac_f32_e32 v42, 0xba000000, v120
	v_pk_mov_b32 v[118:119], v[116:117], v[114:115] op_sel:[1,0]
	v_mov_b32_e32 v117, v115
	v_fmamk_f32 v43, v120, 0xba000000, v43
	v_fmac_f32_e32 v38, 0xba000000, v120
	v_mul_f32_e32 v0, v42, v42
	v_pk_add_f32 v[114:115], v[118:119], v[116:117]
	v_fmamk_f32 v39, v120, 0xba000000, v39
	v_pk_fma_f32 v[116:117], v[42:43], v[42:43], v[0:1] op_sel_hi:[1,1,0]
	v_mul_f32_e32 v0, v38, v38
	v_pk_add_f32 v[40:41], v[40:41], v[40:41] op_sel_hi:[0,1]
	v_pk_add_f32 v[114:115], v[114:115], v[114:115] op_sel_hi:[0,1]
	v_pk_fma_f32 v[118:119], v[38:39], v[38:39], v[0:1] op_sel_hi:[1,1,0]
	v_fmamk_f32 v35, v120, 0xba000000, v35
	v_fmac_f32_e32 v34, 0xba000000, v120
	v_fmamk_f32 v37, v120, 0xba000000, v37
	v_fmac_f32_e32 v36, 0xba000000, v120
	v_mul_f32_e32 v116, v36, v36
	v_mul_f32_e32 v118, v37, v37
	v_mul_f32_e32 v114, v34, v34
	v_mul_f32_e32 v40, v35, v35
	v_pk_add_f32 v[116:117], v[116:117], v[118:119]
	v_pk_add_f32 v[40:41], v[114:115], v[40:41]
	s_nop 0
	v_pk_add_f32 v[40:41], v[116:117], v[40:41]
	s_nop 0
	v_add_f32_e32 v0, v40, v41
	ds_bpermute_b32 v40, v146, v0
	s_waitcnt lgkmcnt(0)
	v_add_f32_e32 v0, v0, v40
	ds_bpermute_b32 v40, v147, v0
	s_waitcnt lgkmcnt(0)
	v_add_f32_e32 v0, v0, v40
	ds_bpermute_b32 v40, v148, v0
	s_waitcnt lgkmcnt(0)
	v_add_f32_e32 v0, v0, v40
	ds_bpermute_b32 v40, v149, v0
	s_waitcnt lgkmcnt(0)
	v_add_f32_e32 v0, v0, v40
	ds_bpermute_b32 v40, v150, v0
	s_waitcnt lgkmcnt(0)
	v_add_f32_e32 v0, v0, v40
	ds_bpermute_b32 v40, v151, v0
	s_waitcnt lgkmcnt(0)
	v_add_f32_e32 v0, v0, v40
	v_fmamk_f32 v0, v0, 0x3a000000, v225
	v_cmp_gt_f32_e32 vcc, s80, v0
	v_mul_f32_e32 v40, 0x4f800000, v0
	s_nop 0
	v_cndmask_b32_e32 v0, v0, v40, vcc
	v_sqrt_f32_e32 v40, v0
	s_nop 0
	v_add_u32_e32 v41, -1, v40
	v_fma_f32 v114, -v41, v40, v0
	v_cmp_ge_f32_e64 s[46:47], 0, v114
	v_add_u32_e32 v114, 1, v40
	s_nop 0
	v_cndmask_b32_e64 v41, v40, v41, s[46:47]
	v_fma_f32 v40, -v114, v40, v0
	v_cmp_lt_f32_e64 s[46:47], 0, v40
	s_nop 1
	v_cndmask_b32_e64 v40, v41, v114, s[46:47]
	v_mul_f32_e32 v41, 0x37800000, v40
	v_cndmask_b32_e32 v40, v40, v41, vcc
	v_cmp_class_f32_e32 vcc, v0, v226
	s_nop 1
	v_cndmask_b32_e32 v0, v40, v0, vcc
	v_div_scale_f32 v40, s[4:5], v0, v0, 1.0
	v_rcp_f32_e32 v41, v40
	s_brev_b32 s4, 48
	v_fma_f32 v114, -v40, v41, 1.0
	v_fmac_f32_e32 v41, v114, v41
	v_div_scale_f32 v114, vcc, 1.0, v0, 1.0
	v_mul_f32_e32 v115, v114, v41
	v_fma_f32 v116, -v40, v115, v114
	v_fmac_f32_e32 v115, v116, v41
	v_fma_f32 v40, -v40, v115, v114
	v_div_fmas_f32 v40, v40, v41, v115
	v_div_fixup_f32 v0, v40, v0, 1.0
	v_pk_mul_f32 v[40:41], v[112:113], v[0:1] op_sel_hi:[1,0]
	ds_read_b128 v[112:115], v152
	ds_read_b128 v[116:119], v152 offset:16
	ds_read_b128 v[120:123], v152 offset:8192
	v_pk_mul_f32 v[62:63], v[62:63], v[0:1] op_sel_hi:[1,0]
	v_pk_mul_f32 v[58:59], v[58:59], v[0:1] op_sel_hi:[1,0]
	v_pk_mul_f32 v[54:55], v[54:55], v[0:1] op_sel_hi:[1,0]
	v_pk_mul_f32 v[46:47], v[46:47], v[0:1] op_sel_hi:[1,0]
	s_waitcnt lgkmcnt(0)
	v_pk_fma_f32 v[114:115], v[114:115], v[62:63], v[122:123]
	v_pk_fma_f32 v[112:113], v[112:113], v[40:41], v[120:121]
	v_pk_mul_f32 v[40:41], v[64:65], v[0:1] op_sel_hi:[1,0]
	v_pk_mul_f32 v[64:65], v[60:61], v[0:1] op_sel_hi:[1,0]
	ds_read_b128 v[60:63], v152 offset:8208
	v_pk_mul_f32 v[38:39], v[38:39], v[0:1] op_sel_hi:[1,0]
	s_waitcnt lgkmcnt(0)
	v_pk_fma_f32 v[64:65], v[118:119], v[64:65], v[62:63]
	v_pk_fma_f32 v[116:117], v[116:117], v[40:41], v[60:61]
	v_add_co_u32_e32 v40, vcc, s4, v110
	v_cvt_pk_bf16_f32 v60, v112, v113
	v_cvt_pk_bf16_f32 v61, v114, v115
	v_cvt_pk_bf16_f32 v62, v116, v117
	v_cvt_pk_bf16_f32 v63, v64, v65
	v_addc_co_u32_e32 v41, vcc, 0, v111, vcc
	global_store_dwordx4 v[40:41], v[60:63], off
	v_lshlrev_b32_e32 v118, 16, v60
	v_and_b32_e32 v119, 0xffff0000, v60
	v_lshlrev_b32_e32 v60, 16, v61
	v_and_b32_e32 v61, 0xffff0000, v61
	v_pk_add_f32 v[112:113], v[112:113], v[118:119] neg_lo:[0,1] neg_hi:[0,1]
	v_pk_add_f32 v[60:61], v[114:115], v[60:61] neg_lo:[0,1] neg_hi:[0,1]
	v_cvt_pk_bf16_f32 v112, v112, v113
	v_cvt_pk_bf16_f32 v113, v60, v61
	v_lshlrev_b32_e32 v60, 16, v62
	v_and_b32_e32 v61, 0xffff0000, v62
	v_pk_add_f32 v[60:61], v[116:117], v[60:61] neg_lo:[0,1] neg_hi:[0,1]
	s_brev_b32 s4, 32
	v_cvt_pk_bf16_f32 v114, v60, v61
	v_lshlrev_b32_e32 v60, 16, v63
	v_and_b32_e32 v61, 0xffff0000, v63
	v_pk_add_f32 v[60:61], v[64:65], v[60:61] neg_lo:[0,1] neg_hi:[0,1]
	s_nop 0
	v_cvt_pk_bf16_f32 v115, v60, v61
	v_add_co_u32_e32 v60, vcc, s4, v110
	s_nop 1
	v_addc_co_u32_e32 v61, vcc, 0, v111, vcc
	global_store_dwordx4 v[60:61], v[112:115], off
	ds_read_b128 v[62:65], v152 offset:2048
	ds_read_b128 v[112:115], v152 offset:10240
	s_waitcnt lgkmcnt(0)
	v_pk_fma_f32 v[64:65], v[64:65], v[54:55], v[114:115]
	v_pk_fma_f32 v[62:63], v[62:63], v[58:59], v[112:113]
	v_pk_mul_f32 v[112:113], v[56:57], v[0:1] op_sel_hi:[1,0]
	v_pk_mul_f32 v[114:115], v[52:53], v[0:1] op_sel_hi:[1,0]
	ds_read_b128 v[52:55], v152 offset:2064
	ds_read_b128 v[56:59], v152 offset:10256
	s_waitcnt lgkmcnt(0)
	v_pk_fma_f32 v[56:57], v[52:53], v[112:113], v[56:57]
	v_cvt_pk_bf16_f32 v52, v62, v63
	v_pk_fma_f32 v[58:59], v[54:55], v[114:115], v[58:59]
	v_lshlrev_b32_e32 v112, 16, v52
	v_and_b32_e32 v113, 0xffff0000, v52
	v_cvt_pk_bf16_f32 v53, v64, v65
	v_cvt_pk_bf16_f32 v54, v56, v57
	v_cvt_pk_bf16_f32 v55, v58, v59
	v_pk_add_f32 v[62:63], v[62:63], v[112:113] neg_lo:[0,1] neg_hi:[0,1]
	global_store_dwordx4 v[40:41], v[52:55], off offset:1024
	s_nop 1
	v_cvt_pk_bf16_f32 v52, v62, v63
	v_lshlrev_b32_e32 v62, 16, v53
	v_and_b32_e32 v63, 0xffff0000, v53
	v_pk_add_f32 v[62:63], v[64:65], v[62:63] neg_lo:[0,1] neg_hi:[0,1]
	s_nop 0
	v_cvt_pk_bf16_f32 v53, v62, v63
	v_lshlrev_b32_e32 v62, 16, v54
	v_and_b32_e32 v63, 0xffff0000, v54
	v_pk_add_f32 v[56:57], v[56:57], v[62:63] neg_lo:[0,1] neg_hi:[0,1]
	s_nop 0
	v_cvt_pk_bf16_f32 v54, v56, v57
	v_lshlrev_b32_e32 v56, 16, v55
	v_and_b32_e32 v57, 0xffff0000, v55
	v_pk_add_f32 v[56:57], v[58:59], v[56:57] neg_lo:[0,1] neg_hi:[0,1]
	v_pk_mul_f32 v[58:59], v[50:51], v[0:1] op_sel_hi:[1,0]
	v_cvt_pk_bf16_f32 v55, v56, v57
	global_store_dwordx4 v[60:61], v[52:55], off offset:1024
	ds_read_b128 v[50:53], v152 offset:4096
	ds_read_b128 v[54:57], v152 offset:12288
	s_waitcnt lgkmcnt(0)
	v_pk_fma_f32 v[52:53], v[52:53], v[46:47], v[56:57]
	v_pk_fma_f32 v[54:55], v[50:51], v[58:59], v[54:55]
	v_pk_mul_f32 v[56:57], v[48:49], v[0:1] op_sel_hi:[1,0]
	v_pk_mul_f32 v[58:59], v[44:45], v[0:1] op_sel_hi:[1,0]
	ds_read_b128 v[44:47], v152 offset:4112
	ds_read_b128 v[48:51], v152 offset:12304
	s_waitcnt lgkmcnt(0)
	v_pk_fma_f32 v[48:49], v[44:45], v[56:57], v[48:49]
	v_cvt_pk_bf16_f32 v44, v54, v55
	v_pk_fma_f32 v[50:51], v[46:47], v[58:59], v[50:51]
	v_lshlrev_b32_e32 v56, 16, v44
	v_and_b32_e32 v57, 0xffff0000, v44
	v_cvt_pk_bf16_f32 v45, v52, v53
	v_cvt_pk_bf16_f32 v46, v48, v49
	v_cvt_pk_bf16_f32 v47, v50, v51
	v_pk_add_f32 v[54:55], v[54:55], v[56:57] neg_lo:[0,1] neg_hi:[0,1]
	global_store_dwordx4 v[40:41], v[44:47], off offset:2048
	s_nop 1
	v_cvt_pk_bf16_f32 v44, v54, v55
	v_lshlrev_b32_e32 v54, 16, v45
	v_and_b32_e32 v55, 0xffff0000, v45
	v_pk_add_f32 v[52:53], v[52:53], v[54:55] neg_lo:[0,1] neg_hi:[0,1]
	v_pk_mul_f32 v[54:55], v[42:43], v[0:1] op_sel_hi:[1,0]
	v_cvt_pk_bf16_f32 v45, v52, v53
	v_lshlrev_b32_e32 v52, 16, v46
	v_and_b32_e32 v53, 0xffff0000, v46
	v_pk_add_f32 v[48:49], v[48:49], v[52:53] neg_lo:[0,1] neg_hi:[0,1]
	s_nop 0
	v_cvt_pk_bf16_f32 v46, v48, v49
	v_lshlrev_b32_e32 v48, 16, v47
	v_and_b32_e32 v49, 0xffff0000, v47
	v_pk_add_f32 v[48:49], v[50:51], v[48:49] neg_lo:[0,1] neg_hi:[0,1]
	s_nop 0
	v_cvt_pk_bf16_f32 v47, v48, v49
	global_store_dwordx4 v[60:61], v[44:47], off offset:2048
	ds_read_b128 v[42:45], v152 offset:6144
	ds_read_b128 v[46:49], v152 offset:6160
	ds_read_b128 v[50:53], v152 offset:14336
	s_waitcnt lgkmcnt(0)
	v_pk_fma_f32 v[38:39], v[44:45], v[38:39], v[52:53]
	v_pk_fma_f32 v[42:43], v[42:43], v[54:55], v[50:51]
	v_pk_mul_f32 v[44:45], v[36:37], v[0:1] op_sel_hi:[1,0]
	v_pk_mul_f32 v[50:51], v[34:35], v[0:1] op_sel_hi:[1,0]
	ds_read_b128 v[34:37], v152 offset:14352
	s_waitcnt lgkmcnt(0)
	v_pk_fma_f32 v[48:49], v[48:49], v[50:51], v[36:37]
	v_pk_fma_f32 v[44:45], v[46:47], v[44:45], v[34:35]
	v_cvt_pk_bf16_f32 v34, v42, v43
	v_cvt_pk_bf16_f32 v35, v38, v39
	v_cvt_pk_bf16_f32 v36, v44, v45
	v_cvt_pk_bf16_f32 v37, v48, v49
	global_store_dwordx4 v[40:41], v[34:37], off offset:3072
	v_lshlrev_b32_e32 v40, 16, v34
	v_and_b32_e32 v41, 0xffff0000, v34
	v_pk_add_f32 v[40:41], v[42:43], v[40:41] neg_lo:[0,1] neg_hi:[0,1]
	s_nop 0
	v_cvt_pk_bf16_f32 v34, v40, v41
	v_lshlrev_b32_e32 v40, 16, v35
	v_and_b32_e32 v41, 0xffff0000, v35
	v_pk_add_f32 v[38:39], v[38:39], v[40:41] neg_lo:[0,1] neg_hi:[0,1]
	s_nop 0
	v_cvt_pk_bf16_f32 v35, v38, v39
	v_lshlrev_b32_e32 v38, 16, v36
	v_and_b32_e32 v39, 0xffff0000, v36
	v_pk_add_f32 v[38:39], v[44:45], v[38:39] neg_lo:[0,1] neg_hi:[0,1]
	s_nop 0
	v_cvt_pk_bf16_f32 v36, v38, v39
	v_lshlrev_b32_e32 v38, 16, v37
	v_and_b32_e32 v39, 0xffff0000, v37
	v_pk_add_f32 v[38:39], v[48:49], v[38:39] neg_lo:[0,1] neg_hi:[0,1]
	s_nop 0
	v_cvt_pk_bf16_f32 v37, v38, v39
	global_store_dwordx4 v[60:61], v[34:37], off offset:3072
	v_lshl_add_u64 v[110:111], v[110:111], 0, s[74:75]
	s_and_b64 vcc, exec, s[48:49]
	s_cbranch_vccnz .LBB0_611
.LBB0_609:
	v_add_co_u32_e32 v34, vcc, 0x10000000, v110
	s_nop 1
	v_addc_co_u32_e32 v35, vcc, 0, v111, vcc
	global_load_dwordx4 v[58:61], v[34:35], off nt
	global_load_dwordx4 v[50:53], v[34:35], off offset:1024 nt
	global_load_dwordx4 v[62:65], v[110:111], off nt
	global_load_dwordx4 v[54:57], v[110:111], off offset:1024 nt
	global_load_dwordx4 v[42:45], v[34:35], off offset:2048 nt
	s_nop 0
	global_load_dwordx4 v[34:37], v[34:35], off offset:3072 nt
	s_nop 0
	global_load_dwordx4 v[46:49], v[110:111], off offset:2048 nt
	global_load_dwordx4 v[38:41], v[110:111], off offset:3072 nt
	s_cmp_eq_u32 s50, 0
	s_cbranch_scc1 .Lln_f0
	s_waitcnt vmcnt(21)
	s_branch .Lln_d0

.Lln_d0:
	v_lshlrev_b32_e32 v112, 16, v10
	v_and_b32_e32 v113, 0xffff0000, v10
	v_lshlrev_b32_e32 v116, 16, v2
	v_and_b32_e32 v117, 0xffff0000, v2
	v_lshlrev_b32_e32 v114, 16, v11
	v_and_b32_e32 v115, 0xffff0000, v11
	v_lshlrev_b32_e32 v118, 16, v3
	v_and_b32_e32 v119, 0xffff0000, v3
	v_pk_fma_f32 v[140:141], v[112:113], s[90:91], v[116:117] op_sel_hi:[1,0,1]
	v_lshlrev_b32_e32 v112, 16, v12
	v_and_b32_e32 v113, 0xffff0000, v12
	v_lshlrev_b32_e32 v116, 16, v4
	v_and_b32_e32 v117, 0xffff0000, v4
	v_pk_fma_f32 v[136:137], v[114:115], s[90:91], v[118:119] op_sel_hi:[1,0,1]
	v_lshlrev_b32_e32 v114, 16, v13
	v_and_b32_e32 v115, 0xffff0000, v13
	v_lshlrev_b32_e32 v118, 16, v5
	v_and_b32_e32 v119, 0xffff0000, v5
	v_pk_fma_f32 v[142:143], v[112:113], s[90:91], v[116:117] op_sel_hi:[1,0,1]
	v_pk_fma_f32 v[138:139], v[114:115], s[90:91], v[118:119] op_sel_hi:[1,0,1]
	v_mov_b32_e32 v112, v142
	v_mov_b32_e32 v113, v140
	v_mov_b32_e32 v114, v143
	v_mov_b32_e32 v115, v141
	v_pk_add_f32 v[112:113], v[112:113], v[114:115]
	v_mov_b32_e32 v114, v138
	v_mov_b32_e32 v115, v136
	v_mov_b32_e32 v116, v139
	v_mov_b32_e32 v117, v137
	v_pk_add_f32 v[114:115], v[114:115], v[116:117]
	v_lshlrev_b32_e32 v116, 16, v6
	v_pk_add_f32 v[112:113], v[112:113], v[114:115]
	s_cmp_eq_u32 s50, 0
	s_cbranch_scc1 .Lln_f1
	s_waitcnt vmcnt(20)
	s_branch .Lln_d1

.Lln_d1:
	v_lshlrev_b32_e32 v114, 16, v15
	v_pk_add_f32 v[144:145], v[112:113], v[112:113] op_sel:[0,1] op_sel_hi:[1,0]
	v_lshlrev_b32_e32 v112, 16, v14
	v_and_b32_e32 v113, 0xffff0000, v14
	v_and_b32_e32 v115, 0xffff0000, v15
	v_and_b32_e32 v117, 0xffff0000, v6
	v_lshlrev_b32_e32 v118, 16, v7
	v_and_b32_e32 v119, 0xffff0000, v7
	v_pk_fma_f32 v[128:129], v[114:115], s[90:91], v[118:119] op_sel_hi:[1,0,1]
	v_pk_fma_f32 v[132:133], v[112:113], s[90:91], v[116:117] op_sel_hi:[1,0,1]
	v_lshlrev_b32_e32 v112, 16, v16
	v_and_b32_e32 v113, 0xffff0000, v16
	v_lshlrev_b32_e32 v114, 16, v17
	v_and_b32_e32 v115, 0xffff0000, v17
	v_lshlrev_b32_e32 v116, 16, v8
	v_and_b32_e32 v117, 0xffff0000, v8
	v_lshlrev_b32_e32 v118, 16, v9
	v_and_b32_e32 v119, 0xffff0000, v9
	v_pk_fma_f32 v[130:131], v[114:115], s[90:91], v[118:119] op_sel_hi:[1,0,1]
	v_pk_fma_f32 v[134:135], v[112:113], s[90:91], v[116:117] op_sel_hi:[1,0,1]
	v_pk_mov_b32 v[112:113], v[132:133], v[128:129] op_sel:[1,0]
	v_mov_b32_e32 v114, v132
	v_mov_b32_e32 v115, v129
	v_pk_add_f32 v[112:113], v[112:113], v[114:115]
	v_mov_b32_e32 v114, v134
	v_pk_add_f32 v[188:189], v[112:113], v[112:113] op_sel:[0,1] op_sel_hi:[1,0]
	v_pk_mov_b32 v[112:113], v[134:135], v[130:131] op_sel:[1,0]
	v_mov_b32_e32 v115, v131
	v_pk_add_f32 v[112:113], v[112:113], v[114:115]
	s_cmp_eq_u32 s50, 0
	s_cbranch_scc1 .Lln_f2
	s_waitcnt vmcnt(17)
	s_branch .Lln_d2

.Lln_d2:
	v_lshlrev_b32_e32 v114, 16, v27
	v_pk_add_f32 v[190:191], v[112:113], v[112:113] op_sel:[0,1] op_sel_hi:[1,0]
	v_lshlrev_b32_e32 v112, 16, v26
	v_and_b32_e32 v113, 0xffff0000, v26
	v_and_b32_e32 v115, 0xffff0000, v27
	v_lshlrev_b32_e32 v116, 16, v18
	v_and_b32_e32 v117, 0xffff0000, v18
	v_lshlrev_b32_e32 v118, 16, v19
	v_and_b32_e32 v119, 0xffff0000, v19
	v_pk_fma_f32 v[120:121], v[114:115], s[90:91], v[118:119] op_sel_hi:[1,0,1]
	v_pk_fma_f32 v[124:125], v[112:113], s[90:91], v[116:117] op_sel_hi:[1,0,1]
	v_lshlrev_b32_e32 v112, 16, v28
	v_and_b32_e32 v113, 0xffff0000, v28
	v_lshlrev_b32_e32 v114, 16, v29
	v_and_b32_e32 v115, 0xffff0000, v29
	v_lshlrev_b32_e32 v116, 16, v20
	v_and_b32_e32 v117, 0xffff0000, v20
	v_lshlrev_b32_e32 v118, 16, v21
	v_and_b32_e32 v119, 0xffff0000, v21
	v_pk_fma_f32 v[122:123], v[114:115], s[90:91], v[118:119] op_sel_hi:[1,0,1]
	v_pk_fma_f32 v[126:127], v[112:113], s[90:91], v[116:117] op_sel_hi:[1,0,1]
	s_cmp_eq_u32 s50, 0
	s_cbranch_scc1 .Lln_f3
	s_waitcnt vmcnt(16)
	s_branch .Lln_d3

.Lln_d3:
	v_lshlrev_b32_e32 v112, 16, v30
	v_and_b32_e32 v113, 0xffff0000, v30
	v_lshlrev_b32_e32 v114, 16, v31
	v_and_b32_e32 v115, 0xffff0000, v31
	v_lshlrev_b32_e32 v116, 16, v22
	v_and_b32_e32 v117, 0xffff0000, v22
	v_lshlrev_b32_e32 v118, 16, v23
	v_and_b32_e32 v119, 0xffff0000, v23
	v_pk_fma_f32 v[114:115], v[114:115], s[90:91], v[118:119] op_sel_hi:[1,0,1]
	v_pk_fma_f32 v[118:119], v[112:113], s[90:91], v[116:117] op_sel_hi:[1,0,1]
	v_lshlrev_b32_e32 v116, 16, v32
	v_and_b32_e32 v117, 0xffff0000, v32
	v_lshlrev_b32_e32 v112, 16, v33
	v_and_b32_e32 v113, 0xffff0000, v33
	v_lshlrev_b32_e32 v204, 16, v24
	v_and_b32_e32 v205, 0xffff0000, v24
	v_lshlrev_b32_e32 v206, 16, v25
	v_and_b32_e32 v207, 0xffff0000, v25
	v_add_f32_e32 v192, v124, v125
	v_add_f32_e32 v194, v120, v121
	v_pk_fma_f32 v[112:113], v[112:113], s[90:91], v[206:207] op_sel_hi:[1,0,1]
	v_pk_fma_f32 v[116:117], v[116:117], s[90:91], v[204:205] op_sel_hi:[1,0,1]
	v_mov_b32_e32 v193, v114
	v_mov_b32_e32 v195, v115
	v_add_f32_e32 v196, v126, v127
	v_add_f32_e32 v202, v122, v123
	v_mov_b32_e32 v197, v118
	v_mov_b32_e32 v203, v119
	v_pk_add_f32 v[192:193], v[192:193], v[194:195]
	v_mov_b32_e32 v145, v116
	v_mov_b32_e32 v194, v1
	v_mov_b32_e32 v195, v117
	v_mov_b32_e32 v191, v112
	v_mov_b32_e32 v189, v113
	v_pk_add_f32 v[196:197], v[196:197], v[202:203]
	v_pk_add_f32 v[144:145], v[144:145], v[194:195]
	v_pk_add_f32 v[188:189], v[190:191], v[188:189]
	v_pk_add_f32 v[192:193], v[196:197], v[192:193]
	v_pk_add_f32 v[144:145], v[144:145], v[188:189]
	s_nop 0
	v_pk_add_f32 v[144:145], v[144:145], v[192:193]
	s_nop 0
	v_add_f32_e32 v0, v144, v145
	ds_bpermute_b32 v144, v146, v0
	s_waitcnt lgkmcnt(0)
	v_add_f32_e32 v0, v0, v144
	ds_bpermute_b32 v144, v147, v0
	s_waitcnt lgkmcnt(0)
	v_add_f32_e32 v0, v0, v144
	ds_bpermute_b32 v144, v148, v0
	s_waitcnt lgkmcnt(0)
	v_add_f32_e32 v0, v0, v144
	ds_bpermute_b32 v144, v149, v0
	s_waitcnt lgkmcnt(0)
	v_add_f32_e32 v0, v0, v144
	ds_bpermute_b32 v144, v150, v0
	s_waitcnt lgkmcnt(0)
	v_add_f32_e32 v0, v0, v144
	ds_bpermute_b32 v144, v151, v0
	s_waitcnt lgkmcnt(0)
	v_add_f32_e32 v187, v0, v144
	v_fmamk_f32 v141, v187, 0xba000000, v141
	v_fmamk_f32 v143, v187, 0xba000000, v143
	v_fmamk_f32 v137, v187, 0xba000000, v137
	v_fmac_f32_e32 v140, 0xba000000, v187
	v_fmamk_f32 v139, v187, 0xba000000, v139
	v_fmac_f32_e32 v142, 0xba000000, v187
	v_mov_b32_e32 v188, v141
	v_mov_b32_e32 v189, v143
	v_fmac_f32_e32 v136, 0xba000000, v187
	v_fmac_f32_e32 v138, 0xba000000, v187
	v_mov_b32_e32 v144, v140
	v_mov_b32_e32 v145, v142
	v_pk_mul_f32 v[188:189], v[188:189], v[188:189]
	v_mov_b32_e32 v190, v137
	v_mov_b32_e32 v191, v139
	v_pk_fma_f32 v[144:145], v[144:145], v[144:145], v[188:189]
	v_mov_b32_e32 v188, v136
	v_mov_b32_e32 v189, v138
	v_pk_mul_f32 v[190:191], v[190:191], v[190:191]
	v_fmamk_f32 v133, v187, 0xba000000, v133
	v_pk_fma_f32 v[188:189], v[188:189], v[188:189], v[190:191]
	v_fmac_f32_e32 v132, 0xba000000, v187
	v_fmamk_f32 v129, v187, 0xba000000, v129
	v_fmac_f32_e32 v128, 0xba000000, v187
	v_pk_add_f32 v[144:145], v[144:145], v[188:189]
	v_pk_mul_f32 v[188:189], v[128:129], v[128:129]
	v_pk_mul_f32 v[190:191], v[132:133], v[132:133]
	v_fmac_f32_e32 v134, 0xba000000, v187
	v_pk_mov_b32 v[192:193], v[190:191], v[188:189] op_sel:[1,0]
	v_mov_b32_e32 v191, v189
	v_fmamk_f32 v135, v187, 0xba000000, v135
	v_fmac_f32_e32 v130, 0xba000000, v187
	v_mul_f32_e32 v0, v134, v134
	v_pk_add_f32 v[188:189], v[192:193], v[190:191]
	v_fmamk_f32 v131, v187, 0xba000000, v131
	v_pk_fma_f32 v[190:191], v[134:135], v[134:135], v[0:1] op_sel_hi:[1,1,0]
	v_mul_f32_e32 v0, v130, v130
	v_pk_add_f32 v[144:145], v[144:145], v[144:145] op_sel_hi:[0,1]
	v_pk_add_f32 v[188:189], v[188:189], v[188:189] op_sel_hi:[0,1]
	v_pk_fma_f32 v[192:193], v[130:131], v[130:131], v[0:1] op_sel_hi:[1,1,0]
	v_fmamk_f32 v121, v187, 0xba000000, v121
	v_fmac_f32_e32 v120, 0xba000000, v187
	v_fmamk_f32 v125, v187, 0xba000000, v125
	v_fmac_f32_e32 v124, 0xba000000, v187
	v_mul_f32_e32 v190, v124, v124
	v_mul_f32_e32 v192, v125, v125
	v_mul_f32_e32 v188, v120, v120
	v_mul_f32_e32 v144, v121, v121
	v_pk_add_f32 v[190:191], v[190:191], v[192:193]
	v_pk_add_f32 v[144:145], v[188:189], v[144:145]
	v_fmamk_f32 v127, v187, 0xba000000, v127
	v_fmac_f32_e32 v126, 0xba000000, v187
	v_fmamk_f32 v123, v187, 0xba000000, v123
	v_fmac_f32_e32 v122, 0xba000000, v187
	v_pk_add_f32 v[144:145], v[190:191], v[144:145]
	v_pk_mul_f32 v[188:189], v[122:123], v[122:123]
	v_pk_mul_f32 v[190:191], v[126:127], v[126:127]
	v_fmac_f32_e32 v118, 0xba000000, v187
	v_pk_mov_b32 v[192:193], v[190:191], v[188:189] op_sel:[1,0]
	v_mov_b32_e32 v191, v189
	v_fmamk_f32 v119, v187, 0xba000000, v119
	v_fmac_f32_e32 v114, 0xba000000, v187
	v_mul_f32_e32 v0, v118, v118
	v_pk_add_f32 v[188:189], v[192:193], v[190:191]
	v_fmamk_f32 v115, v187, 0xba000000, v115
	v_pk_fma_f32 v[190:191], v[118:119], v[118:119], v[0:1] op_sel_hi:[1,1,0]
	v_mul_f32_e32 v0, v114, v114
	v_pk_add_f32 v[144:145], v[144:145], v[144:145] op_sel_hi:[0,1]
	v_pk_add_f32 v[188:189], v[188:189], v[188:189] op_sel_hi:[0,1]
	v_pk_fma_f32 v[192:193], v[114:115], v[114:115], v[0:1] op_sel_hi:[1,1,0]
	v_fmamk_f32 v113, v187, 0xba000000, v113
	v_fmac_f32_e32 v112, 0xba000000, v187
	v_fmamk_f32 v117, v187, 0xba000000, v117
	v_fmac_f32_e32 v116, 0xba000000, v187
	v_mul_f32_e32 v190, v116, v116
	v_mul_f32_e32 v192, v117, v117
	v_mul_f32_e32 v188, v112, v112
	v_mul_f32_e32 v144, v113, v113
	v_pk_add_f32 v[190:191], v[190:191], v[192:193]
	v_pk_add_f32 v[144:145], v[188:189], v[144:145]
	s_nop 0
	v_pk_add_f32 v[144:145], v[190:191], v[144:145]
	s_nop 0
	v_add_f32_e32 v0, v144, v145
	ds_bpermute_b32 v144, v146, v0
	s_waitcnt lgkmcnt(0)
	v_add_f32_e32 v0, v0, v144
	ds_bpermute_b32 v144, v147, v0
	s_waitcnt lgkmcnt(0)
	v_add_f32_e32 v0, v0, v144
	ds_bpermute_b32 v144, v148, v0
	s_waitcnt lgkmcnt(0)
	v_add_f32_e32 v0, v0, v144
	ds_bpermute_b32 v144, v149, v0
	s_waitcnt lgkmcnt(0)
	v_add_f32_e32 v0, v0, v144
	ds_bpermute_b32 v144, v150, v0
	s_waitcnt lgkmcnt(0)
	v_add_f32_e32 v0, v0, v144
	ds_bpermute_b32 v144, v151, v0
	s_waitcnt lgkmcnt(0)
	v_add_f32_e32 v0, v0, v144
	v_fmamk_f32 v0, v0, 0x3a000000, v225
	v_mul_f32_e32 v144, 0x4f800000, v0
	v_cmp_gt_f32_e32 vcc, s80, v0
	s_nop 1
	v_cndmask_b32_e32 v0, v0, v144, vcc
	v_sqrt_f32_e32 v144, v0
	s_nop 0
	v_add_u32_e32 v145, -1, v144
	v_fma_f32 v187, -v145, v144, v0
	v_cmp_ge_f32_e64 s[46:47], 0, v187
	v_add_u32_e32 v187, 1, v144
	s_nop 0
	v_cndmask_b32_e64 v145, v144, v145, s[46:47]
	v_fma_f32 v144, -v187, v144, v0
	v_cmp_lt_f32_e64 s[46:47], 0, v144
	s_nop 1
	v_cndmask_b32_e64 v144, v145, v187, s[46:47]
	v_mul_f32_e32 v145, 0x37800000, v144
	v_cndmask_b32_e32 v144, v144, v145, vcc
	v_cmp_class_f32_e32 vcc, v0, v226
	s_nop 1
	v_cndmask_b32_e32 v0, v144, v0, vcc
	v_div_scale_f32 v144, s[4:5], v0, v0, 1.0
	v_rcp_f32_e32 v145, v144
	s_add_i32 s4, s58, s50
	s_ashr_i32 s5, s4, 31
	s_lshl_b64 s[46:47], s[4:5], 12
	v_fma_f32 v187, -v144, v145, 1.0
	v_fmac_f32_e32 v145, v187, v145
	v_div_scale_f32 v187, vcc, 1.0, v0, 1.0
	v_mul_f32_e32 v188, v187, v145
	v_fma_f32 v189, -v144, v188, v187
	v_fmac_f32_e32 v188, v189, v145
	v_fma_f32 v144, -v144, v188, v187
	v_div_fmas_f32 v144, v144, v145, v188
	ds_read_b128 v[188:191], v152
	ds_read_b128 v[192:195], v152 offset:8192
	ds_read_b128 v[202:205], v152 offset:16
	ds_read_b128 v[206:209], v152 offset:8208
	v_div_fixup_f32 v0, v144, v0, 1.0
	v_pk_mul_f32 v[140:141], v[140:141], v[0:1] op_sel_hi:[1,0]
	v_pk_mul_f32 v[136:137], v[136:137], v[0:1] op_sel_hi:[1,0]
	s_waitcnt lgkmcnt(2)
	v_pk_fma_f32 v[140:141], v[188:189], v[140:141], v[192:193]
	v_pk_fma_f32 v[190:191], v[190:191], v[136:137], v[194:195]
	v_pk_mul_f32 v[136:137], v[142:143], v[0:1] op_sel_hi:[1,0]
	v_pk_mul_f32 v[138:139], v[138:139], v[0:1] op_sel_hi:[1,0]
	s_waitcnt lgkmcnt(0)
	v_pk_fma_f32 v[188:189], v[202:203], v[136:137], v[206:207]
	v_cvt_pk_bf16_f32 v136, v140, v141
	v_pk_fma_f32 v[142:143], v[204:205], v[138:139], v[208:209]
	v_lshlrev_b32_e32 v192, 16, v136
	v_and_b32_e32 v193, 0xffff0000, v136
	v_lshl_add_u64 v[196:197], v[78:79], 0, s[46:47]
	v_cvt_pk_bf16_f32 v137, v190, v191
	v_cvt_pk_bf16_f32 v138, v188, v189
	v_cvt_pk_bf16_f32 v139, v142, v143
	v_pk_add_f32 v[140:141], v[140:141], v[192:193] neg_lo:[0,1] neg_hi:[0,1]
	global_store_dwordx4 v[196:197], v[136:139], off
	v_lshl_add_u64 v[144:145], v[76:77], 0, s[46:47]
	v_pk_mul_f32 v[132:133], v[132:133], v[0:1] op_sel_hi:[1,0]
	v_cvt_pk_bf16_f32 v136, v140, v141
	v_lshlrev_b32_e32 v140, 16, v137
	v_and_b32_e32 v141, 0xffff0000, v137
	v_pk_add_f32 v[140:141], v[190:191], v[140:141] neg_lo:[0,1] neg_hi:[0,1]
	v_pk_mul_f32 v[128:129], v[128:129], v[0:1] op_sel_hi:[1,0]
	v_cvt_pk_bf16_f32 v137, v140, v141
	v_lshlrev_b32_e32 v140, 16, v138
	v_and_b32_e32 v141, 0xffff0000, v138
	v_pk_add_f32 v[140:141], v[188:189], v[140:141] neg_lo:[0,1] neg_hi:[0,1]
	v_pk_mul_f32 v[130:131], v[130:131], v[0:1] op_sel_hi:[1,0]
	v_cvt_pk_bf16_f32 v138, v140, v141
	v_lshlrev_b32_e32 v140, 16, v139
	v_and_b32_e32 v141, 0xffff0000, v139
	v_pk_add_f32 v[140:141], v[142:143], v[140:141] neg_lo:[0,1] neg_hi:[0,1]
	v_pk_mul_f32 v[124:125], v[124:125], v[0:1] op_sel_hi:[1,0]
	v_cvt_pk_bf16_f32 v139, v140, v141
	global_store_dwordx4 v[144:145], v[136:139], off
	ds_read_b128 v[136:139], v152 offset:2048
	ds_read_b128 v[140:143], v152 offset:10240
	ds_read_b128 v[188:191], v152 offset:2064
	ds_read_b128 v[192:195], v152 offset:10256
	v_pk_mul_f32 v[120:121], v[120:121], v[0:1] op_sel_hi:[1,0]
	v_pk_mul_f32 v[122:123], v[122:123], v[0:1] op_sel_hi:[1,0]
	v_pk_mul_f32 v[118:119], v[118:119], v[0:1] op_sel_hi:[1,0]
	s_waitcnt lgkmcnt(2)
	v_pk_fma_f32 v[138:139], v[138:139], v[128:129], v[142:143]
	v_pk_fma_f32 v[132:133], v[136:137], v[132:133], v[140:141]
	v_pk_mul_f32 v[128:129], v[134:135], v[0:1] op_sel_hi:[1,0]
	s_waitcnt lgkmcnt(0)
	v_pk_fma_f32 v[134:135], v[190:191], v[130:131], v[194:195]
	v_pk_fma_f32 v[136:137], v[188:189], v[128:129], v[192:193]
	v_cvt_pk_bf16_f32 v128, v132, v133
	v_lshlrev_b32_e32 v140, 16, v128
	v_and_b32_e32 v141, 0xffff0000, v128
	v_cvt_pk_bf16_f32 v129, v138, v139
	v_cvt_pk_bf16_f32 v130, v136, v137
	v_cvt_pk_bf16_f32 v131, v134, v135
	v_pk_add_f32 v[132:133], v[132:133], v[140:141] neg_lo:[0,1] neg_hi:[0,1]
	global_store_dwordx4 v[196:197], v[128:131], off offset:1024
	v_pk_mul_f32 v[114:115], v[114:115], v[0:1] op_sel_hi:[1,0]
	v_pk_mul_f32 v[112:113], v[112:113], v[0:1] op_sel_hi:[1,0]
	v_cvt_pk_bf16_f32 v128, v132, v133
	v_lshlrev_b32_e32 v132, 16, v129
	v_and_b32_e32 v133, 0xffff0000, v129
	v_pk_add_f32 v[132:133], v[138:139], v[132:133] neg_lo:[0,1] neg_hi:[0,1]
	s_nop 0
	v_cvt_pk_bf16_f32 v129, v132, v133
	v_lshlrev_b32_e32 v132, 16, v130
	v_and_b32_e32 v133, 0xffff0000, v130
	v_pk_add_f32 v[132:133], v[136:137], v[132:133] neg_lo:[0,1] neg_hi:[0,1]
	s_nop 0
	v_cvt_pk_bf16_f32 v130, v132, v133
	v_lshlrev_b32_e32 v132, 16, v131
	v_and_b32_e32 v133, 0xffff0000, v131
	v_pk_add_f32 v[132:133], v[134:135], v[132:133] neg_lo:[0,1] neg_hi:[0,1]
	s_nop 0
	v_cvt_pk_bf16_f32 v131, v132, v133
	global_store_dwordx4 v[144:145], v[128:131], off offset:1024
	ds_read_b128 v[128:131], v152 offset:4096
	ds_read_b128 v[132:135], v152 offset:12288
	ds_read_b128 v[136:139], v152 offset:4112
	ds_read_b128 v[140:143], v152 offset:12304
	s_waitcnt lgkmcnt(2)
	v_pk_fma_f32 v[130:131], v[130:131], v[120:121], v[134:135]
	v_pk_fma_f32 v[124:125], v[128:129], v[124:125], v[132:133]
	v_pk_mul_f32 v[120:121], v[126:127], v[0:1] op_sel_hi:[1,0]
	s_waitcnt lgkmcnt(0)
	v_pk_fma_f32 v[126:127], v[138:139], v[122:123], v[142:143]
	v_pk_fma_f32 v[128:129], v[136:137], v[120:121], v[140:141]
	v_cvt_pk_bf16_f32 v120, v124, v125
	v_lshlrev_b32_e32 v132, 16, v120
	v_and_b32_e32 v133, 0xffff0000, v120
	v_cvt_pk_bf16_f32 v121, v130, v131
	v_cvt_pk_bf16_f32 v122, v128, v129
	v_cvt_pk_bf16_f32 v123, v126, v127
	v_pk_add_f32 v[124:125], v[124:125], v[132:133] neg_lo:[0,1] neg_hi:[0,1]
	global_store_dwordx4 v[196:197], v[120:123], off offset:2048
	s_nop 1
	v_cvt_pk_bf16_f32 v120, v124, v125
	v_lshlrev_b32_e32 v124, 16, v121
	v_and_b32_e32 v125, 0xffff0000, v121
	v_pk_add_f32 v[124:125], v[130:131], v[124:125] neg_lo:[0,1] neg_hi:[0,1]
	s_nop 0
	v_cvt_pk_bf16_f32 v121, v124, v125
	v_lshlrev_b32_e32 v124, 16, v122
	v_and_b32_e32 v125, 0xffff0000, v122
	v_pk_add_f32 v[124:125], v[128:129], v[124:125] neg_lo:[0,1] neg_hi:[0,1]
	s_nop 0
	v_cvt_pk_bf16_f32 v122, v124, v125
	v_lshlrev_b32_e32 v124, 16, v123
	v_and_b32_e32 v125, 0xffff0000, v123
	v_pk_add_f32 v[124:125], v[126:127], v[124:125] neg_lo:[0,1] neg_hi:[0,1]
	s_nop 0
	v_cvt_pk_bf16_f32 v123, v124, v125
	global_store_dwordx4 v[144:145], v[120:123], off offset:2048
	ds_read_b128 v[120:123], v152 offset:6144
	ds_read_b128 v[124:127], v152 offset:14336
	ds_read_b128 v[128:131], v152 offset:6160
	ds_read_b128 v[132:135], v152 offset:14352
	s_waitcnt lgkmcnt(2)
	v_pk_fma_f32 v[118:119], v[120:121], v[118:119], v[124:125]
	v_pk_fma_f32 v[122:123], v[122:123], v[114:115], v[126:127]
	v_pk_mul_f32 v[114:115], v[116:117], v[0:1] op_sel_hi:[1,0]
	s_waitcnt lgkmcnt(0)
	v_pk_fma_f32 v[116:117], v[130:131], v[112:113], v[134:135]
	v_cvt_pk_bf16_f32 v112, v118, v119
	v_pk_fma_f32 v[120:121], v[128:129], v[114:115], v[132:133]
	v_lshlrev_b32_e32 v124, 16, v112
	v_and_b32_e32 v125, 0xffff0000, v112
	v_cvt_pk_bf16_f32 v113, v122, v123
	v_cvt_pk_bf16_f32 v114, v120, v121
	v_cvt_pk_bf16_f32 v115, v116, v117
	v_pk_add_f32 v[118:119], v[118:119], v[124:125] neg_lo:[0,1] neg_hi:[0,1]
	global_store_dwordx4 v[196:197], v[112:115], off offset:3072
	s_nop 1
	v_cvt_pk_bf16_f32 v112, v118, v119
	v_lshlrev_b32_e32 v118, 16, v113
	v_and_b32_e32 v119, 0xffff0000, v113
	v_pk_add_f32 v[118:119], v[122:123], v[118:119] neg_lo:[0,1] neg_hi:[0,1]
	s_nop 0
	v_cvt_pk_bf16_f32 v113, v118, v119
	v_lshlrev_b32_e32 v118, 16, v114
	v_and_b32_e32 v119, 0xffff0000, v114
	v_pk_add_f32 v[118:119], v[120:121], v[118:119] neg_lo:[0,1] neg_hi:[0,1]
	s_nop 0
	v_cvt_pk_bf16_f32 v114, v118, v119
	v_lshlrev_b32_e32 v118, 16, v115
	v_and_b32_e32 v119, 0xffff0000, v115
	v_pk_add_f32 v[116:117], v[116:117], v[118:119] neg_lo:[0,1] neg_hi:[0,1]
	s_nop 0
	v_cvt_pk_bf16_f32 v115, v116, v117
	global_store_dwordx4 v[144:145], v[112:115], off offset:3072
	s_cmp_gt_u32 s50, 5
	s_cselect_b64 s[48:49], -1, 0
	s_and_b64 vcc, exec, s[48:49]
	s_cbranch_vccnz .LBB0_608
	s_add_i32 s4, s4, 2
	s_ashr_i32 s5, s4, 31
	s_lshl_b64 s[4:5], s[4:5], 12
	v_lshl_add_u64 v[22:23], v[72:73], 0, s[4:5]
	v_lshl_add_u64 v[30:31], v[74:75], 0, s[4:5]
	global_load_dwordx4 v[2:5], v[22:23], off nt
	global_load_dwordx4 v[6:9], v[22:23], off offset:1024 nt
	global_load_dwordx4 v[10:13], v[30:31], off nt
	global_load_dwordx4 v[14:17], v[30:31], off offset:1024 nt
	global_load_dwordx4 v[18:21], v[22:23], off offset:2048 nt
	s_nop 0
	global_load_dwordx4 v[22:25], v[22:23], off offset:3072 nt
	s_nop 0
	global_load_dwordx4 v[26:29], v[30:31], off offset:2048 nt
	s_nop 0
	global_load_dwordx4 v[30:33], v[30:31], off offset:3072 nt
	s_branch .LBB0_608
